# speedup vs baseline: 1.0183x; 1.0046x over previous
.Ldn_loop:
	s_waitcnt lgkmcnt(0)
	v_mfma_f32_16x16x32_bf16 v[64:67], v[176:179], v[160:163], v[64:67]
	ds_read_b128 v[200:203], v11 offset:0
	v_mfma_f32_16x16x32_bf16 v[68:71], v[176:179], v[164:167], v[68:71]
	s_add_u32 m0, s20, 0x5000
	v_mfma_f32_16x16x32_bf16 v[72:75], v[176:179], v[168:171], v[72:75]
	ds_read_b128 v[204:207], v11 offset:2048
	v_mfma_f32_16x16x32_bf16 v[76:79], v[176:179], v[172:175], v[76:79]
	global_load_lds_dwordx4 v3, s[18:19]
	v_mfma_f32_16x16x32_bf16 v[80:83], v[180:183], v[160:163], v[80:83]
	ds_read_b128 v[208:211], v11 offset:4096
	v_mfma_f32_16x16x32_bf16 v[84:87], v[180:183], v[164:167], v[84:87]
	s_add_u32 m0, s20, 0x6000
	v_mfma_f32_16x16x32_bf16 v[88:91], v[180:183], v[168:171], v[88:91]
	ds_read_b128 v[212:215], v11 offset:6144
	v_mfma_f32_16x16x32_bf16 v[92:95], v[180:183], v[172:175], v[92:95]
	global_load_lds_dwordx4 v4, s[18:19]
	v_mfma_f32_16x16x32_bf16 v[96:99], v[184:187], v[160:163], v[96:99]
	ds_read_b128 v[216:219], v13 offset:0
	v_mfma_f32_16x16x32_bf16 v[100:103], v[184:187], v[164:167], v[100:103]
	s_add_u32 m0, s20, 0x7000
	v_mfma_f32_16x16x32_bf16 v[104:107], v[184:187], v[168:171], v[104:107]
	ds_read_b128 v[220:223], v13 offset:2048
	v_mfma_f32_16x16x32_bf16 v[108:111], v[184:187], v[172:175], v[108:111]
	global_load_lds_dwordx4 v5, s[18:19]
	v_mfma_f32_16x16x32_bf16 v[112:115], v[188:191], v[160:163], v[112:115]
	ds_read_b128 v[224:227], v13 offset:4096
	v_mfma_f32_16x16x32_bf16 v[116:119], v[188:191], v[164:167], v[116:119]
	s_add_u32 m0, s20, 0x8000
	v_mfma_f32_16x16x32_bf16 v[120:123], v[188:191], v[168:171], v[120:123]
	ds_read_b128 v[228:231], v13 offset:6144
	v_mfma_f32_16x16x32_bf16 v[124:127], v[188:191], v[172:175], v[124:127]
	global_load_lds_dwordx4 v6, s[18:19]
	v_mfma_f32_16x16x32_bf16 v[128:131], v[192:195], v[160:163], v[128:131]
	ds_read_b128 v[232:235], v13 offset:8192
	v_mfma_f32_16x16x32_bf16 v[132:135], v[192:195], v[164:167], v[132:135]
	s_add_u32 m0, s20, 0x9000
	v_mfma_f32_16x16x32_bf16 v[136:139], v[192:195], v[168:171], v[136:139]
	ds_read_b128 v[236:239], v13 offset:10240
	v_mfma_f32_16x16x32_bf16 v[140:143], v[192:195], v[172:175], v[140:143]
	global_load_lds_dwordx4 v7, s[18:19]
	v_mfma_f32_16x16x32_bf16 v[144:147], v[196:199], v[160:163], v[144:147]
	s_add_u32 s16, s16, 0x80
	s_addc_u32 s17, s17, 0
	s_add_u32 s18, s18, 0x80
	s_addc_u32 s19, s19, 0
	v_mfma_f32_16x16x32_bf16 v[148:151], v[196:199], v[164:167], v[148:151]
	s_add_u32 s20, s20, 0xa000
	s_sub_u32 s22, s20, 0x28000
	s_cmp_ge_u32 s20, 0x28000
	s_cselect_b32 s20, s22, s20
	v_mfma_f32_16x16x32_bf16 v[152:155], v[196:199], v[168:171], v[152:155]
	v_add_u32_e32 v10, s21, v8
	v_add_u32_e32 v12, s21, v9
	v_xor_b32_e32 v11, 64, v10
	v_xor_b32_e32 v13, 64, v12
	v_mfma_f32_16x16x32_bf16 v[156:159], v[196:199], v[172:175], v[156:159]
	s_add_u32 s21, s21, 0xa000
	s_sub_u32 s23, s21, 0x28000
	s_cmp_ge_u32 s21, 0x28000
	s_cselect_b32 s21, s23, s21
	s_waitcnt vmcnt(20) lgkmcnt(0)
	s_barrier
	v_mfma_f32_16x16x32_bf16 v[64:67], v[216:219], v[200:203], v[64:67]
	ds_read_b128 v[160:163], v10 offset:0
	v_mfma_f32_16x16x32_bf16 v[68:71], v[216:219], v[204:207], v[68:71]
	s_add_u32 m0, s20, 0x0
	v_mfma_f32_16x16x32_bf16 v[72:75], v[216:219], v[208:211], v[72:75]
	ds_read_b128 v[164:167], v10 offset:2048
	v_mfma_f32_16x16x32_bf16 v[76:79], v[216:219], v[212:215], v[76:79]
	global_load_lds_dwordx4 v2, s[16:17]
	v_mfma_f32_16x16x32_bf16 v[80:83], v[220:223], v[200:203], v[80:83]
	ds_read_b128 v[168:171], v10 offset:4096
	v_mfma_f32_16x16x32_bf16 v[84:87], v[220:223], v[204:207], v[84:87]
	s_add_u32 m0, s20, 0x1000
	v_mfma_f32_16x16x32_bf16 v[88:91], v[220:223], v[208:211], v[88:91]
	ds_read_b128 v[172:175], v10 offset:6144
	v_mfma_f32_16x16x32_bf16 v[92:95], v[220:223], v[212:215], v[92:95]
	global_load_lds_dwordx4 v3, s[16:17]
	v_mfma_f32_16x16x32_bf16 v[96:99], v[224:227], v[200:203], v[96:99]
	ds_read_b128 v[176:179], v12 offset:0
	v_mfma_f32_16x16x32_bf16 v[100:103], v[224:227], v[204:207], v[100:103]
	s_add_u32 m0, s20, 0x2000
	v_mfma_f32_16x16x32_bf16 v[104:107], v[224:227], v[208:211], v[104:107]
	ds_read_b128 v[180:183], v12 offset:2048
	v_mfma_f32_16x16x32_bf16 v[108:111], v[224:227], v[212:215], v[108:111]
	global_load_lds_dwordx4 v4, s[16:17]
	v_mfma_f32_16x16x32_bf16 v[112:115], v[228:231], v[200:203], v[112:115]
	ds_read_b128 v[184:187], v12 offset:4096
	v_mfma_f32_16x16x32_bf16 v[116:119], v[228:231], v[204:207], v[116:119]
	s_add_u32 m0, s20, 0x3000
	v_mfma_f32_16x16x32_bf16 v[120:123], v[228:231], v[208:211], v[120:123]
	ds_read_b128 v[188:191], v12 offset:6144
	v_mfma_f32_16x16x32_bf16 v[124:127], v[228:231], v[212:215], v[124:127]
	global_load_lds_dwordx4 v5, s[16:17]
	v_mfma_f32_16x16x32_bf16 v[128:131], v[232:235], v[200:203], v[128:131]
	ds_read_b128 v[192:195], v12 offset:8192
	v_mfma_f32_16x16x32_bf16 v[132:135], v[232:235], v[204:207], v[132:135]
	s_add_u32 m0, s20, 0x4000
	v_mfma_f32_16x16x32_bf16 v[136:139], v[232:235], v[208:211], v[136:139]
	ds_read_b128 v[196:199], v12 offset:10240
	v_mfma_f32_16x16x32_bf16 v[140:143], v[232:235], v[212:215], v[140:143]
	global_load_lds_dwordx4 v2, s[18:19]
	v_mfma_f32_16x16x32_bf16 v[144:147], v[236:239], v[200:203], v[144:147]
	v_mfma_f32_16x16x32_bf16 v[148:151], v[236:239], v[204:207], v[148:151]
	v_mfma_f32_16x16x32_bf16 v[152:155], v[236:239], v[208:211], v[152:155]
	v_mfma_f32_16x16x32_bf16 v[156:159], v[236:239], v[212:215], v[156:159]
	s_add_u32 s15, s15, 1
	s_cmp_lt_u32 s15, 44
	s_cbranch_scc1 .Ldn_loop
	s_waitcnt lgkmcnt(0)
	v_mfma_f32_16x16x32_bf16 v[64:67], v[176:179], v[160:163], v[64:67]
	ds_read_b128 v[200:203], v11 offset:0
	v_mfma_f32_16x16x32_bf16 v[68:71], v[176:179], v[164:167], v[68:71]
	s_add_u32 m0, s20, 0x5000
	v_mfma_f32_16x16x32_bf16 v[72:75], v[176:179], v[168:171], v[72:75]
	ds_read_b128 v[204:207], v11 offset:2048
	v_mfma_f32_16x16x32_bf16 v[76:79], v[176:179], v[172:175], v[76:79]
	global_load_lds_dwordx4 v3, s[18:19]
	v_mfma_f32_16x16x32_bf16 v[80:83], v[180:183], v[160:163], v[80:83]
	ds_read_b128 v[208:211], v11 offset:4096
	v_mfma_f32_16x16x32_bf16 v[84:87], v[180:183], v[164:167], v[84:87]
	s_add_u32 m0, s20, 0x6000
	v_mfma_f32_16x16x32_bf16 v[88:91], v[180:183], v[168:171], v[88:91]
	ds_read_b128 v[212:215], v11 offset:6144
	v_mfma_f32_16x16x32_bf16 v[92:95], v[180:183], v[172:175], v[92:95]
	global_load_lds_dwordx4 v4, s[18:19]
	v_mfma_f32_16x16x32_bf16 v[96:99], v[184:187], v[160:163], v[96:99]
	ds_read_b128 v[216:219], v13 offset:0
	v_mfma_f32_16x16x32_bf16 v[100:103], v[184:187], v[164:167], v[100:103]
	s_add_u32 m0, s20, 0x7000
	v_mfma_f32_16x16x32_bf16 v[104:107], v[184:187], v[168:171], v[104:107]
	ds_read_b128 v[220:223], v13 offset:2048
	v_mfma_f32_16x16x32_bf16 v[108:111], v[184:187], v[172:175], v[108:111]
	global_load_lds_dwordx4 v5, s[18:19]
	v_mfma_f32_16x16x32_bf16 v[112:115], v[188:191], v[160:163], v[112:115]
	ds_read_b128 v[224:227], v13 offset:4096
	v_mfma_f32_16x16x32_bf16 v[116:119], v[188:191], v[164:167], v[116:119]
	s_add_u32 m0, s20, 0x8000
	v_mfma_f32_16x16x32_bf16 v[120:123], v[188:191], v[168:171], v[120:123]
	ds_read_b128 v[228:231], v13 offset:6144
	v_mfma_f32_16x16x32_bf16 v[124:127], v[188:191], v[172:175], v[124:127]
	global_load_lds_dwordx4 v6, s[18:19]
	v_mfma_f32_16x16x32_bf16 v[128:131], v[192:195], v[160:163], v[128:131]
	ds_read_b128 v[232:235], v13 offset:8192
	v_mfma_f32_16x16x32_bf16 v[132:135], v[192:195], v[164:167], v[132:135]
	s_add_u32 m0, s20, 0x9000
	v_mfma_f32_16x16x32_bf16 v[136:139], v[192:195], v[168:171], v[136:139]
	ds_read_b128 v[236:239], v13 offset:10240
	v_mfma_f32_16x16x32_bf16 v[140:143], v[192:195], v[172:175], v[140:143]
	global_load_lds_dwordx4 v7, s[18:19]
	v_mfma_f32_16x16x32_bf16 v[144:147], v[196:199], v[160:163], v[144:147]
	s_add_u32 s16, s16, 0x80
	s_addc_u32 s17, s17, 0
	s_add_u32 s18, s18, 0x80
	s_addc_u32 s19, s19, 0
	v_mfma_f32_16x16x32_bf16 v[148:151], v[196:199], v[164:167], v[148:151]
	s_add_u32 s20, s20, 0xa000
	s_sub_u32 s22, s20, 0x28000
	s_cmp_ge_u32 s20, 0x28000
	s_cselect_b32 s20, s22, s20
	v_mfma_f32_16x16x32_bf16 v[152:155], v[196:199], v[168:171], v[152:155]
	v_add_u32_e32 v10, s21, v8
	v_add_u32_e32 v12, s21, v9
	v_xor_b32_e32 v11, 64, v10
	v_xor_b32_e32 v13, 64, v12
	v_mfma_f32_16x16x32_bf16 v[156:159], v[196:199], v[172:175], v[156:159]
	s_add_u32 s21, s21, 0xa000
	s_sub_u32 s23, s21, 0x28000
	s_cmp_ge_u32 s21, 0x28000
	s_cselect_b32 s21, s23, s21
	s_waitcnt vmcnt(20) lgkmcnt(0)
	s_barrier
	v_mfma_f32_16x16x32_bf16 v[64:67], v[216:219], v[200:203], v[64:67]
	ds_read_b128 v[160:163], v10 offset:0
	v_mfma_f32_16x16x32_bf16 v[68:71], v[216:219], v[204:207], v[68:71]
	ds_read_b128 v[164:167], v10 offset:2048
	v_mfma_f32_16x16x32_bf16 v[72:75], v[216:219], v[208:211], v[72:75]
	ds_read_b128 v[168:171], v10 offset:4096
	v_mfma_f32_16x16x32_bf16 v[76:79], v[216:219], v[212:215], v[76:79]
	ds_read_b128 v[172:175], v10 offset:6144
	v_mfma_f32_16x16x32_bf16 v[80:83], v[220:223], v[200:203], v[80:83]
	ds_read_b128 v[176:179], v12 offset:0
	v_mfma_f32_16x16x32_bf16 v[84:87], v[220:223], v[204:207], v[84:87]
	ds_read_b128 v[180:183], v12 offset:2048
	v_mfma_f32_16x16x32_bf16 v[88:91], v[220:223], v[208:211], v[88:91]
	ds_read_b128 v[184:187], v12 offset:4096
	v_mfma_f32_16x16x32_bf16 v[92:95], v[220:223], v[212:215], v[92:95]
	ds_read_b128 v[188:191], v12 offset:6144
	v_mfma_f32_16x16x32_bf16 v[96:99], v[224:227], v[200:203], v[96:99]
	ds_read_b128 v[192:195], v12 offset:8192
	v_mfma_f32_16x16x32_bf16 v[100:103], v[224:227], v[204:207], v[100:103]
	ds_read_b128 v[196:199], v12 offset:10240
	v_mfma_f32_16x16x32_bf16 v[104:107], v[224:227], v[208:211], v[104:107]
	v_mfma_f32_16x16x32_bf16 v[108:111], v[224:227], v[212:215], v[108:111]
	v_mfma_f32_16x16x32_bf16 v[112:115], v[228:231], v[200:203], v[112:115]
	v_mfma_f32_16x16x32_bf16 v[116:119], v[228:231], v[204:207], v[116:119]
	v_mfma_f32_16x16x32_bf16 v[120:123], v[228:231], v[208:211], v[120:123]
	v_mfma_f32_16x16x32_bf16 v[124:127], v[228:231], v[212:215], v[124:127]
	v_mfma_f32_16x16x32_bf16 v[128:131], v[232:235], v[200:203], v[128:131]
	v_mfma_f32_16x16x32_bf16 v[132:135], v[232:235], v[204:207], v[132:135]
	v_mfma_f32_16x16x32_bf16 v[136:139], v[232:235], v[208:211], v[136:139]
	v_mfma_f32_16x16x32_bf16 v[140:143], v[232:235], v[212:215], v[140:143]
	v_mfma_f32_16x16x32_bf16 v[144:147], v[236:239], v[200:203], v[144:147]
	v_mfma_f32_16x16x32_bf16 v[148:151], v[236:239], v[204:207], v[148:151]
	v_mfma_f32_16x16x32_bf16 v[152:155], v[236:239], v[208:211], v[152:155]
	v_mfma_f32_16x16x32_bf16 v[156:159], v[236:239], v[212:215], v[156:159]
	s_waitcnt lgkmcnt(0)
	v_mfma_f32_16x16x32_bf16 v[64:67], v[176:179], v[160:163], v[64:67]
	ds_read_b128 v[200:203], v11 offset:0
	v_mfma_f32_16x16x32_bf16 v[68:71], v[176:179], v[164:167], v[68:71]
	ds_read_b128 v[204:207], v11 offset:2048
	v_mfma_f32_16x16x32_bf16 v[72:75], v[176:179], v[168:171], v[72:75]
	ds_read_b128 v[208:211], v11 offset:4096
	v_mfma_f32_16x16x32_bf16 v[76:79], v[176:179], v[172:175], v[76:79]
	ds_read_b128 v[212:215], v11 offset:6144
	v_mfma_f32_16x16x32_bf16 v[80:83], v[180:183], v[160:163], v[80:83]
	ds_read_b128 v[216:219], v13 offset:0
	v_mfma_f32_16x16x32_bf16 v[84:87], v[180:183], v[164:167], v[84:87]
	ds_read_b128 v[220:223], v13 offset:2048
	v_mfma_f32_16x16x32_bf16 v[88:91], v[180:183], v[168:171], v[88:91]
	ds_read_b128 v[224:227], v13 offset:4096
	v_mfma_f32_16x16x32_bf16 v[92:95], v[180:183], v[172:175], v[92:95]
	ds_read_b128 v[228:231], v13 offset:6144
	v_mfma_f32_16x16x32_bf16 v[96:99], v[184:187], v[160:163], v[96:99]
	ds_read_b128 v[232:235], v13 offset:8192
	v_mfma_f32_16x16x32_bf16 v[100:103], v[184:187], v[164:167], v[100:103]
	ds_read_b128 v[236:239], v13 offset:10240
	v_mfma_f32_16x16x32_bf16 v[104:107], v[184:187], v[168:171], v[104:107]
	v_mfma_f32_16x16x32_bf16 v[108:111], v[184:187], v[172:175], v[108:111]
	v_mfma_f32_16x16x32_bf16 v[112:115], v[188:191], v[160:163], v[112:115]
	v_mfma_f32_16x16x32_bf16 v[116:119], v[188:191], v[164:167], v[116:119]
	v_mfma_f32_16x16x32_bf16 v[120:123], v[188:191], v[168:171], v[120:123]
	v_mfma_f32_16x16x32_bf16 v[124:127], v[188:191], v[172:175], v[124:127]
	v_mfma_f32_16x16x32_bf16 v[128:131], v[192:195], v[160:163], v[128:131]
	v_mfma_f32_16x16x32_bf16 v[132:135], v[192:195], v[164:167], v[132:135]
	v_mfma_f32_16x16x32_bf16 v[136:139], v[192:195], v[168:171], v[136:139]
	v_mfma_f32_16x16x32_bf16 v[140:143], v[192:195], v[172:175], v[140:143]
	v_mfma_f32_16x16x32_bf16 v[144:147], v[196:199], v[160:163], v[144:147]
	v_add_u32_e32 v10, s21, v8
	v_add_u32_e32 v12, s21, v9
	v_xor_b32_e32 v11, 64, v10
	v_xor_b32_e32 v13, 64, v12
	v_mfma_f32_16x16x32_bf16 v[148:151], v[196:199], v[164:167], v[148:151]
	s_add_u32 s21, s21, 0xa000
	s_sub_u32 s23, s21, 0x28000
	s_cmp_ge_u32 s21, 0x28000
	s_cselect_b32 s21, s23, s21
	v_mfma_f32_16x16x32_bf16 v[152:155], v[196:199], v[168:171], v[152:155]
	v_mfma_f32_16x16x32_bf16 v[156:159], v[196:199], v[172:175], v[156:159]
	s_waitcnt vmcnt(10) lgkmcnt(0)
	s_barrier
	v_mfma_f32_16x16x32_bf16 v[64:67], v[216:219], v[200:203], v[64:67]
	ds_read_b128 v[160:163], v10 offset:0
	v_mfma_f32_16x16x32_bf16 v[68:71], v[216:219], v[204:207], v[68:71]
	ds_read_b128 v[164:167], v10 offset:2048
	v_mfma_f32_16x16x32_bf16 v[72:75], v[216:219], v[208:211], v[72:75]
	ds_read_b128 v[168:171], v10 offset:4096
	v_mfma_f32_16x16x32_bf16 v[76:79], v[216:219], v[212:215], v[76:79]
	ds_read_b128 v[172:175], v10 offset:6144
	v_mfma_f32_16x16x32_bf16 v[80:83], v[220:223], v[200:203], v[80:83]
	ds_read_b128 v[176:179], v12 offset:0
	v_mfma_f32_16x16x32_bf16 v[84:87], v[220:223], v[204:207], v[84:87]
	ds_read_b128 v[180:183], v12 offset:2048
	v_mfma_f32_16x16x32_bf16 v[88:91], v[220:223], v[208:211], v[88:91]
	ds_read_b128 v[184:187], v12 offset:4096
	v_mfma_f32_16x16x32_bf16 v[92:95], v[220:223], v[212:215], v[92:95]
	ds_read_b128 v[188:191], v12 offset:6144
	v_mfma_f32_16x16x32_bf16 v[96:99], v[224:227], v[200:203], v[96:99]
	ds_read_b128 v[192:195], v12 offset:8192
	v_mfma_f32_16x16x32_bf16 v[100:103], v[224:227], v[204:207], v[100:103]
	ds_read_b128 v[196:199], v12 offset:10240
	v_mfma_f32_16x16x32_bf16 v[104:107], v[224:227], v[208:211], v[104:107]
	v_mfma_f32_16x16x32_bf16 v[108:111], v[224:227], v[212:215], v[108:111]
	v_mfma_f32_16x16x32_bf16 v[112:115], v[228:231], v[200:203], v[112:115]
	v_mfma_f32_16x16x32_bf16 v[116:119], v[228:231], v[204:207], v[116:119]
	v_mfma_f32_16x16x32_bf16 v[120:123], v[228:231], v[208:211], v[120:123]
	v_mfma_f32_16x16x32_bf16 v[124:127], v[228:231], v[212:215], v[124:127]
	v_mfma_f32_16x16x32_bf16 v[128:131], v[232:235], v[200:203], v[128:131]
	v_mfma_f32_16x16x32_bf16 v[132:135], v[232:235], v[204:207], v[132:135]
	v_mfma_f32_16x16x32_bf16 v[136:139], v[232:235], v[208:211], v[136:139]
	v_mfma_f32_16x16x32_bf16 v[140:143], v[232:235], v[212:215], v[140:143]
	v_mfma_f32_16x16x32_bf16 v[144:147], v[236:239], v[200:203], v[144:147]
	v_mfma_f32_16x16x32_bf16 v[148:151], v[236:239], v[204:207], v[148:151]
	v_mfma_f32_16x16x32_bf16 v[152:155], v[236:239], v[208:211], v[152:155]
	v_mfma_f32_16x16x32_bf16 v[156:159], v[236:239], v[212:215], v[156:159]
	s_waitcnt lgkmcnt(0)
	v_mfma_f32_16x16x32_bf16 v[64:67], v[176:179], v[160:163], v[64:67]
	ds_read_b128 v[200:203], v11 offset:0
	v_mfma_f32_16x16x32_bf16 v[68:71], v[176:179], v[164:167], v[68:71]
	ds_read_b128 v[204:207], v11 offset:2048
	v_mfma_f32_16x16x32_bf16 v[72:75], v[176:179], v[168:171], v[72:75]
	ds_read_b128 v[208:211], v11 offset:4096
	v_mfma_f32_16x16x32_bf16 v[76:79], v[176:179], v[172:175], v[76:79]
	ds_read_b128 v[212:215], v11 offset:6144
	v_mfma_f32_16x16x32_bf16 v[80:83], v[180:183], v[160:163], v[80:83]
	ds_read_b128 v[216:219], v13 offset:0
	v_mfma_f32_16x16x32_bf16 v[84:87], v[180:183], v[164:167], v[84:87]
	ds_read_b128 v[220:223], v13 offset:2048
	v_mfma_f32_16x16x32_bf16 v[88:91], v[180:183], v[168:171], v[88:91]
	ds_read_b128 v[224:227], v13 offset:4096
	v_mfma_f32_16x16x32_bf16 v[92:95], v[180:183], v[172:175], v[92:95]
	ds_read_b128 v[228:231], v13 offset:6144
	v_mfma_f32_16x16x32_bf16 v[96:99], v[184:187], v[160:163], v[96:99]
	ds_read_b128 v[232:235], v13 offset:8192
	v_mfma_f32_16x16x32_bf16 v[100:103], v[184:187], v[164:167], v[100:103]
	ds_read_b128 v[236:239], v13 offset:10240
	v_mfma_f32_16x16x32_bf16 v[104:107], v[184:187], v[168:171], v[104:107]
	v_mfma_f32_16x16x32_bf16 v[108:111], v[184:187], v[172:175], v[108:111]
	v_mfma_f32_16x16x32_bf16 v[112:115], v[188:191], v[160:163], v[112:115]
	v_mfma_f32_16x16x32_bf16 v[116:119], v[188:191], v[164:167], v[116:119]
	v_mfma_f32_16x16x32_bf16 v[120:123], v[188:191], v[168:171], v[120:123]
	v_mfma_f32_16x16x32_bf16 v[124:127], v[188:191], v[172:175], v[124:127]
	v_mfma_f32_16x16x32_bf16 v[128:131], v[192:195], v[160:163], v[128:131]
	v_mfma_f32_16x16x32_bf16 v[132:135], v[192:195], v[164:167], v[132:135]
	v_mfma_f32_16x16x32_bf16 v[136:139], v[192:195], v[168:171], v[136:139]
	v_mfma_f32_16x16x32_bf16 v[140:143], v[192:195], v[172:175], v[140:143]
	v_mfma_f32_16x16x32_bf16 v[144:147], v[196:199], v[160:163], v[144:147]
	v_add_u32_e32 v10, s21, v8
	v_add_u32_e32 v12, s21, v9
	v_xor_b32_e32 v11, 64, v10
	v_xor_b32_e32 v13, 64, v12
	v_mfma_f32_16x16x32_bf16 v[148:151], v[196:199], v[164:167], v[148:151]
	s_add_u32 s21, s21, 0xa000
	s_sub_u32 s23, s21, 0x28000
	s_cmp_ge_u32 s21, 0x28000
	s_cselect_b32 s21, s23, s21
	v_mfma_f32_16x16x32_bf16 v[152:155], v[196:199], v[168:171], v[152:155]
	v_mfma_f32_16x16x32_bf16 v[156:159], v[196:199], v[172:175], v[156:159]
	s_waitcnt vmcnt(0) lgkmcnt(0)
	s_barrier
	v_mfma_f32_16x16x32_bf16 v[64:67], v[216:219], v[200:203], v[64:67]
	ds_read_b128 v[160:163], v10 offset:0
	v_mfma_f32_16x16x32_bf16 v[68:71], v[216:219], v[204:207], v[68:71]
	global_load_dwordx4 v[16:19], v56, s[8:9] offset:0
	v_mfma_f32_16x16x32_bf16 v[72:75], v[216:219], v[208:211], v[72:75]
	ds_read_b128 v[164:167], v10 offset:2048
	v_mfma_f32_16x16x32_bf16 v[76:79], v[216:219], v[212:215], v[76:79]
	global_load_dwordx4 v[20:23], v57, s[8:9] offset:0
	v_mfma_f32_16x16x32_bf16 v[80:83], v[220:223], v[200:203], v[80:83]
	ds_read_b128 v[168:171], v10 offset:4096
	v_mfma_f32_16x16x32_bf16 v[84:87], v[220:223], v[204:207], v[84:87]
	global_load_dwordx4 v[24:27], v58, s[8:9] offset:0
	v_mfma_f32_16x16x32_bf16 v[88:91], v[220:223], v[208:211], v[88:91]
	ds_read_b128 v[172:175], v10 offset:6144
	v_mfma_f32_16x16x32_bf16 v[92:95], v[220:223], v[212:215], v[92:95]
	global_load_dwordx4 v[28:31], v59, s[8:9] offset:0
	v_mfma_f32_16x16x32_bf16 v[96:99], v[224:227], v[200:203], v[96:99]
	ds_read_b128 v[176:179], v12 offset:0
	v_mfma_f32_16x16x32_bf16 v[100:103], v[224:227], v[204:207], v[100:103]
	global_load_dwordx4 v[32:35], v56, s[8:9] offset:64
	v_mfma_f32_16x16x32_bf16 v[104:107], v[224:227], v[208:211], v[104:107]
	ds_read_b128 v[180:183], v12 offset:2048
	v_mfma_f32_16x16x32_bf16 v[108:111], v[224:227], v[212:215], v[108:111]
	global_load_dwordx4 v[36:39], v57, s[8:9] offset:64
	v_mfma_f32_16x16x32_bf16 v[112:115], v[228:231], v[200:203], v[112:115]
	ds_read_b128 v[184:187], v12 offset:4096
	v_mfma_f32_16x16x32_bf16 v[116:119], v[228:231], v[204:207], v[116:119]
	global_load_dwordx4 v[40:43], v58, s[8:9] offset:64
	v_mfma_f32_16x16x32_bf16 v[120:123], v[228:231], v[208:211], v[120:123]
	ds_read_b128 v[188:191], v12 offset:6144
	v_mfma_f32_16x16x32_bf16 v[124:127], v[228:231], v[212:215], v[124:127]
	global_load_dwordx4 v[44:47], v59, s[8:9] offset:64
	v_mfma_f32_16x16x32_bf16 v[128:131], v[232:235], v[200:203], v[128:131]
	ds_read_b128 v[192:195], v12 offset:8192
	v_mfma_f32_16x16x32_bf16 v[132:135], v[232:235], v[204:207], v[132:135]
	global_load_dwordx4 v[48:51], v56, s[8:9] offset:128
	v_mfma_f32_16x16x32_bf16 v[136:139], v[232:235], v[208:211], v[136:139]
	ds_read_b128 v[196:199], v12 offset:10240
	v_mfma_f32_16x16x32_bf16 v[140:143], v[232:235], v[212:215], v[140:143]
	global_load_dwordx4 v[52:55], v57, s[8:9] offset:128
	v_mfma_f32_16x16x32_bf16 v[144:147], v[236:239], v[200:203], v[144:147]
	global_load_dwordx4 v[240:243], v58, s[8:9] offset:128
	v_mfma_f32_16x16x32_bf16 v[148:151], v[236:239], v[204:207], v[148:151]
	global_load_dwordx4 v[244:247], v59, s[8:9] offset:128
	v_mfma_f32_16x16x32_bf16 v[152:155], v[236:239], v[208:211], v[152:155]
	global_load_dwordx4 v[248:251], v56, s[8:9] offset:192
	v_mfma_f32_16x16x32_bf16 v[156:159], v[236:239], v[212:215], v[156:159]
	global_load_dwordx4 v[252:255], v57, s[8:9] offset:192
	s_waitcnt lgkmcnt(0)
	v_mfma_f32_16x16x32_bf16 v[64:67], v[176:179], v[160:163], v[64:67]
	ds_read_b128 v[200:203], v11 offset:0
	v_mfma_f32_16x16x32_bf16 v[68:71], v[176:179], v[164:167], v[68:71]
	ds_read_b128 v[204:207], v11 offset:2048
	v_mfma_f32_16x16x32_bf16 v[72:75], v[176:179], v[168:171], v[72:75]
	ds_read_b128 v[208:211], v11 offset:4096
	v_mfma_f32_16x16x32_bf16 v[76:79], v[176:179], v[172:175], v[76:79]
	ds_read_b128 v[212:215], v11 offset:6144
	v_mfma_f32_16x16x32_bf16 v[80:83], v[180:183], v[160:163], v[80:83]
	ds_read_b128 v[216:219], v13 offset:0
	v_mfma_f32_16x16x32_bf16 v[84:87], v[180:183], v[164:167], v[84:87]
	ds_read_b128 v[220:223], v13 offset:2048
	v_mfma_f32_16x16x32_bf16 v[88:91], v[180:183], v[168:171], v[88:91]
	ds_read_b128 v[224:227], v13 offset:4096
	v_mfma_f32_16x16x32_bf16 v[92:95], v[180:183], v[172:175], v[92:95]
	ds_read_b128 v[228:231], v13 offset:6144
	v_mfma_f32_16x16x32_bf16 v[96:99], v[184:187], v[160:163], v[96:99]
	ds_read_b128 v[232:235], v13 offset:8192
	v_mfma_f32_16x16x32_bf16 v[100:103], v[184:187], v[164:167], v[100:103]
	ds_read_b128 v[236:239], v13 offset:10240
	v_mfma_f32_16x16x32_bf16 v[104:107], v[184:187], v[168:171], v[104:107]
	v_mfma_f32_16x16x32_bf16 v[108:111], v[184:187], v[172:175], v[108:111]
	v_mfma_f32_16x16x32_bf16 v[112:115], v[188:191], v[160:163], v[112:115]
	v_mfma_f32_16x16x32_bf16 v[116:119], v[188:191], v[164:167], v[116:119]
	v_mfma_f32_16x16x32_bf16 v[120:123], v[188:191], v[168:171], v[120:123]
	v_mfma_f32_16x16x32_bf16 v[124:127], v[188:191], v[172:175], v[124:127]
	v_mfma_f32_16x16x32_bf16 v[128:131], v[192:195], v[160:163], v[128:131]
	v_mfma_f32_16x16x32_bf16 v[132:135], v[192:195], v[164:167], v[132:135]
	v_mfma_f32_16x16x32_bf16 v[136:139], v[192:195], v[168:171], v[136:139]
	v_mfma_f32_16x16x32_bf16 v[140:143], v[192:195], v[172:175], v[140:143]
	v_mfma_f32_16x16x32_bf16 v[144:147], v[196:199], v[160:163], v[144:147]
	v_mfma_f32_16x16x32_bf16 v[148:151], v[196:199], v[164:167], v[148:151]
	v_mfma_f32_16x16x32_bf16 v[152:155], v[196:199], v[168:171], v[152:155]
	v_mfma_f32_16x16x32_bf16 v[156:159], v[196:199], v[172:175], v[156:159]
	s_waitcnt lgkmcnt(0)
	v_mfma_f32_16x16x32_bf16 v[64:67], v[216:219], v[200:203], v[64:67]
	v_mfma_f32_16x16x32_bf16 v[68:71], v[216:219], v[204:207], v[68:71]
	global_load_dwordx4 v[160:163], v58, s[8:9] offset:192
	v_mfma_f32_16x16x32_bf16 v[72:75], v[216:219], v[208:211], v[72:75]
	v_mfma_f32_16x16x32_bf16 v[76:79], v[216:219], v[212:215], v[76:79]
	global_load_dwordx4 v[164:167], v59, s[8:9] offset:192
	v_mfma_f32_16x16x32_bf16 v[80:83], v[220:223], v[200:203], v[80:83]
	v_mfma_f32_16x16x32_bf16 v[84:87], v[220:223], v[204:207], v[84:87]
	global_load_dwordx4 v[168:171], v56, s[8:9] offset:256
	v_mfma_f32_16x16x32_bf16 v[88:91], v[220:223], v[208:211], v[88:91]
	v_mfma_f32_16x16x32_bf16 v[92:95], v[220:223], v[212:215], v[92:95]
	global_load_dwordx4 v[172:175], v57, s[8:9] offset:256
	v_mfma_f32_16x16x32_bf16 v[96:99], v[224:227], v[200:203], v[96:99]
	v_mfma_f32_16x16x32_bf16 v[100:103], v[224:227], v[204:207], v[100:103]
	global_load_dwordx4 v[176:179], v58, s[8:9] offset:256
	v_mfma_f32_16x16x32_bf16 v[104:107], v[224:227], v[208:211], v[104:107]
	v_mfma_f32_16x16x32_bf16 v[108:111], v[224:227], v[212:215], v[108:111]
	global_load_dwordx4 v[180:183], v59, s[8:9] offset:256
	v_mfma_f32_16x16x32_bf16 v[112:115], v[228:231], v[200:203], v[112:115]
	v_mfma_f32_16x16x32_bf16 v[116:119], v[228:231], v[204:207], v[116:119]
	global_load_dwordx4 v[184:187], v56, s[8:9] offset:320
	v_mfma_f32_16x16x32_bf16 v[120:123], v[228:231], v[208:211], v[120:123]
	v_mfma_f32_16x16x32_bf16 v[124:127], v[228:231], v[212:215], v[124:127]
	global_load_dwordx4 v[188:191], v57, s[8:9] offset:320
	v_mfma_f32_16x16x32_bf16 v[128:131], v[232:235], v[200:203], v[128:131]
	v_mfma_f32_16x16x32_bf16 v[132:135], v[232:235], v[204:207], v[132:135]
	global_load_dwordx4 v[192:195], v58, s[8:9] offset:320
	v_mfma_f32_16x16x32_bf16 v[136:139], v[232:235], v[208:211], v[136:139]
	v_mfma_f32_16x16x32_bf16 v[140:143], v[232:235], v[212:215], v[140:143]
	global_load_dwordx4 v[196:199], v59, s[8:9] offset:320
	v_mfma_f32_16x16x32_bf16 v[144:147], v[236:239], v[200:203], v[144:147]
	v_mfma_f32_16x16x32_bf16 v[148:151], v[236:239], v[204:207], v[148:151]
	v_mfma_f32_16x16x32_bf16 v[152:155], v[236:239], v[208:211], v[152:155]
	v_mfma_f32_16x16x32_bf16 v[156:159], v[236:239], v[212:215], v[156:159]
	s_waitcnt vmcnt(23)
	v_pk_add_f32 v[64:65], v[64:65], v[16:17]
	v_pk_add_f32 v[66:67], v[66:67], v[18:19]
	global_store_dwordx4 v56, v[64:67], s[10:11] offset:0
	s_waitcnt vmcnt(23)
	v_pk_add_f32 v[68:69], v[68:69], v[20:21]
	v_pk_add_f32 v[70:71], v[70:71], v[22:23]
	global_store_dwordx4 v57, v[68:71], s[10:11] offset:0
	s_waitcnt vmcnt(23)
	v_pk_add_f32 v[72:73], v[72:73], v[24:25]
	v_pk_add_f32 v[74:75], v[74:75], v[26:27]
	global_store_dwordx4 v58, v[72:75], s[10:11] offset:0
	s_waitcnt vmcnt(23)
	v_pk_add_f32 v[76:77], v[76:77], v[28:29]
	v_pk_add_f32 v[78:79], v[78:79], v[30:31]
	global_store_dwordx4 v59, v[76:79], s[10:11] offset:0
	s_waitcnt vmcnt(23)
	v_pk_add_f32 v[80:81], v[80:81], v[32:33]
	v_pk_add_f32 v[82:83], v[82:83], v[34:35]
	global_store_dwordx4 v56, v[80:83], s[10:11] offset:64
	s_waitcnt vmcnt(23)
	v_pk_add_f32 v[84:85], v[84:85], v[36:37]
	v_pk_add_f32 v[86:87], v[86:87], v[38:39]
	global_store_dwordx4 v57, v[84:87], s[10:11] offset:64
	s_waitcnt vmcnt(23)
	v_pk_add_f32 v[88:89], v[88:89], v[40:41]
	v_pk_add_f32 v[90:91], v[90:91], v[42:43]
	global_store_dwordx4 v58, v[88:91], s[10:11] offset:64
	s_waitcnt vmcnt(23)
	v_pk_add_f32 v[92:93], v[92:93], v[44:45]
	v_pk_add_f32 v[94:95], v[94:95], v[46:47]
	global_store_dwordx4 v59, v[92:95], s[10:11] offset:64
	s_waitcnt vmcnt(23)
	v_pk_add_f32 v[96:97], v[96:97], v[48:49]
	v_pk_add_f32 v[98:99], v[98:99], v[50:51]
	global_store_dwordx4 v56, v[96:99], s[10:11] offset:128
	s_waitcnt vmcnt(23)
	v_pk_add_f32 v[100:101], v[100:101], v[52:53]
	v_pk_add_f32 v[102:103], v[102:103], v[54:55]
	global_store_dwordx4 v57, v[100:103], s[10:11] offset:128
	s_waitcnt vmcnt(23)
	v_pk_add_f32 v[104:105], v[104:105], v[240:241]
	v_pk_add_f32 v[106:107], v[106:107], v[242:243]
	global_store_dwordx4 v58, v[104:107], s[10:11] offset:128
	s_waitcnt vmcnt(23)
	v_pk_add_f32 v[108:109], v[108:109], v[244:245]
	v_pk_add_f32 v[110:111], v[110:111], v[246:247]
	global_store_dwordx4 v59, v[108:111], s[10:11] offset:128
	s_waitcnt vmcnt(23)
	v_pk_add_f32 v[112:113], v[112:113], v[248:249]
	v_pk_add_f32 v[114:115], v[114:115], v[250:251]
	global_store_dwordx4 v56, v[112:115], s[10:11] offset:192
	s_waitcnt vmcnt(23)
	v_pk_add_f32 v[116:117], v[116:117], v[252:253]
	v_pk_add_f32 v[118:119], v[118:119], v[254:255]
	global_store_dwordx4 v57, v[116:119], s[10:11] offset:192
	s_waitcnt vmcnt(23)
	v_pk_add_f32 v[120:121], v[120:121], v[160:161]
	v_pk_add_f32 v[122:123], v[122:123], v[162:163]
	global_store_dwordx4 v58, v[120:123], s[10:11] offset:192
	s_waitcnt vmcnt(23)
	v_pk_add_f32 v[124:125], v[124:125], v[164:165]
	v_pk_add_f32 v[126:127], v[126:127], v[166:167]
	global_store_dwordx4 v59, v[124:127], s[10:11] offset:192
	s_waitcnt vmcnt(23)
	v_pk_add_f32 v[128:129], v[128:129], v[168:169]
	v_pk_add_f32 v[130:131], v[130:131], v[170:171]
	global_store_dwordx4 v56, v[128:131], s[10:11] offset:256
	s_waitcnt vmcnt(23)
	v_pk_add_f32 v[132:133], v[132:133], v[172:173]
	v_pk_add_f32 v[134:135], v[134:135], v[174:175]
	global_store_dwordx4 v57, v[132:135], s[10:11] offset:256
	s_waitcnt vmcnt(23)
	v_pk_add_f32 v[136:137], v[136:137], v[176:177]
	v_pk_add_f32 v[138:139], v[138:139], v[178:179]
	global_store_dwordx4 v58, v[136:139], s[10:11] offset:256
	s_waitcnt vmcnt(23)
	v_pk_add_f32 v[140:141], v[140:141], v[180:181]
	v_pk_add_f32 v[142:143], v[142:143], v[182:183]
	global_store_dwordx4 v59, v[140:143], s[10:11] offset:256
	s_waitcnt vmcnt(23)
	v_pk_add_f32 v[144:145], v[144:145], v[184:185]
	v_pk_add_f32 v[146:147], v[146:147], v[186:187]
	global_store_dwordx4 v56, v[144:147], s[10:11] offset:320
	s_waitcnt vmcnt(23)
	v_pk_add_f32 v[148:149], v[148:149], v[188:189]
	v_pk_add_f32 v[150:151], v[150:151], v[190:191]
	global_store_dwordx4 v57, v[148:151], s[10:11] offset:320
	s_waitcnt vmcnt(23)
	v_pk_add_f32 v[152:153], v[152:153], v[192:193]
	v_pk_add_f32 v[154:155], v[154:155], v[194:195]
	global_store_dwordx4 v58, v[152:155], s[10:11] offset:320
	s_waitcnt vmcnt(23)
	v_pk_add_f32 v[156:157], v[156:157], v[196:197]
	v_pk_add_f32 v[158:159], v[158:159], v[198:199]
	global_store_dwordx4 v59, v[156:159], s[10:11] offset:320
